# nt cache hint on the adaLN GEMV weight stream (phase 0) and the phase-1 x row loads; on top of v47
# speedup vs baseline: 1.0090x; 1.0090x over previous
; #define GAS __attribute__((address_space(1)))
; #define LAS __attribute__((address_space(3)))
; __device__ __forceinline__ void phase0(KP kp, LAS unsigned char* lds, int wave, int bid, int G) {
;     ...
;     for (int u = bid; u < 256; u += G) {
;         const int nc = u & 15, kr = u >> 4, n0 = 768 * nc, k0 = 128 * kr;
;         const float* cvec = (const float*)KIN(1); const float* wada = (const float*)KIN(3);
;         f32x4 acc[3] = {(f32x4){0.f, 0.f, 0.f, 0.f}, (f32x4){0.f, 0.f, 0.f, 0.f}, (f32x4){0.f, 0.f, 0.f, 0.f}};
; #pragma unroll 4
;         for (int i = 0; i < 16; ++i) { const int k = k0 + wave + 8 * i; const float cv = cvec[k]; const float s = cv / (1.0f + __expf(-cv));
;             const float* p = wada + (size_t)k * 12288 + n0 + 4 * lane;
; #pragma unroll
;             for (int q = 0; q < 3; ++q) acc[q] += s * *(const GAS f32x4*)(p + 256 * q); }
;         LAS float* red = (LAS float*)lds;
; #pragma unroll
;         for (int q = 0; q < 3; ++q) *(LAS f32x4*)(red + wave * 768 + 256 * q + 4 * lane) = acc[q];
;         __syncthreads();
;         if (tid < 192) { f32x4 s = *(LAS f32x4*)(red + 4 * tid);
; #pragma unroll
;             for (int w = 1; w < 8; ++w) s += *(LAS f32x4*)(red + w * 768 + 4 * tid);
;             *(GAS f32x4*)((float*)(ws + WS_MODP) + (size_t)kr * 12288 + n0 + 4 * tid) = s; }
;         __syncthreads();
;     }
.LBB0_19:
	s_add_i32 s8, s30, s14
	s_ashr_i32 s9, s8, 31
	v_mad_i64_i32 v[36:37], s[6:7], s8, v21, v[18:19]
	s_lshl_b64 s[6:7], s[8:9], 2
	s_add_u32 s6, s28, s6
	s_addc_u32 s7, s29, s7
	global_load_dwordx4 v[24:27], v[36:37], off nt
	global_load_dwordx4 v[28:31], v[36:37], off offset:1024 nt
	global_load_dwordx4 v[32:35], v[36:37], off offset:2048 nt
	global_load_dword v23, v20, s[6:7]
	global_load_dword v65, v20, s[34:35] offset:-32
	global_load_dword v80, v20, s[34:35]
	global_load_dword v81, v20, s[34:35] offset:32
	s_add_i32 s9, s8, 8
	s_add_i32 s10, s8, 16
	s_add_i32 s8, s8, 24
	v_mad_i64_i32 v[74:75], s[6:7], s9, v21, v[18:19]
	v_mad_i64_i32 v[76:77], s[6:7], s10, v21, v[18:19]
	v_mad_i64_i32 v[78:79], s[6:7], s8, v21, v[18:19]
	global_load_dwordx4 v[36:39], v[74:75], off nt
	global_load_dwordx4 v[40:43], v[74:75], off offset:1024 nt
	global_load_dwordx4 v[44:47], v[74:75], off offset:2048 nt
	global_load_dwordx4 v[48:51], v[76:77], off nt
	global_load_dwordx4 v[52:55], v[76:77], off offset:1024 nt
	global_load_dwordx4 v[56:59], v[76:77], off offset:2048 nt
	global_load_dwordx4 v[60:63], v[78:79], off nt
	global_load_dwordx4 v[66:69], v[78:79], off offset:1024 nt
	global_load_dwordx4 v[70:73], v[78:79], off offset:2048 nt
	s_add_i32 s14, s14, 32
	s_add_u32 s34, s34, 0x80
	s_addc_u32 s35, s35, 0
	s_cmpk_eq_i32 s14, 0x80
	s_waitcnt vmcnt(12)
	v_mul_f32_e32 v74, 0xbfb8aa3b, v23
	s_waitcnt vmcnt(11)
	v_mul_f32_e32 v75, 0xbfb8aa3b, v65
	v_exp_f32_e32 v74, v74
	s_waitcnt vmcnt(10)
	v_mul_f32_e32 v76, 0xbfb8aa3b, v80
	v_exp_f32_e32 v75, v75
	s_waitcnt vmcnt(9)
	v_mul_f32_e32 v77, 0xbfb8aa3b, v81
	v_exp_f32_e32 v76, v76
	v_exp_f32_e32 v77, v77
	v_add_f32_e32 v74, 1.0, v74
	v_add_f32_e32 v75, 1.0, v75
	v_div_scale_f32 v78, s[6:7], v74, v74, v23
	v_add_f32_e32 v76, 1.0, v76
	v_div_scale_f32 v82, s[6:7], v75, v75, v65
	v_rcp_f32_e32 v88, v78
	v_add_f32_e32 v77, 1.0, v77
	v_div_scale_f32 v84, s[8:9], v76, v76, v80
	v_rcp_f32_e32 v89, v82
	v_div_scale_f32 v86, s[10:11], v77, v77, v81
	v_rcp_f32_e32 v90, v84
	v_rcp_f32_e32 v91, v86
	v_fma_f32 v92, -v78, v88, 1.0
	v_div_scale_f32 v79, vcc, v23, v74, v23
	v_fma_f32 v93, -v82, v89, 1.0
	v_fmac_f32_e32 v88, v92, v88
	v_div_scale_f32 v83, s[6:7], v65, v75, v65
	v_fma_f32 v94, -v84, v90, 1.0
	v_fmac_f32_e32 v89, v93, v89
	v_mul_f32_e32 v92, v79, v88
	v_div_scale_f32 v85, s[8:9], v80, v76, v80
	v_fma_f32 v95, -v86, v91, 1.0
	v_fmac_f32_e32 v90, v94, v90
	v_mul_f32_e32 v93, v83, v89
	v_fma_f32 v96, -v78, v92, v79
	v_div_scale_f32 v87, s[10:11], v81, v77, v81
	v_fmac_f32_e32 v91, v95, v91
	v_mul_f32_e32 v94, v85, v90
	v_fma_f32 v97, -v82, v93, v83
	v_fmac_f32_e32 v92, v96, v88
	v_mul_f32_e32 v95, v87, v91
	v_fma_f32 v98, -v84, v94, v85
	v_fmac_f32_e32 v93, v97, v89
	v_fma_f32 v78, -v78, v92, v79
	v_fma_f32 v99, -v86, v95, v87
	v_fmac_f32_e32 v94, v98, v90
	v_fma_f32 v79, -v82, v93, v83
	v_div_fmas_f32 v78, v78, v88, v92
	s_mov_b64 vcc, s[6:7]
	v_fmac_f32_e32 v95, v99, v91
	v_fma_f32 v82, -v84, v94, v85
	v_div_fixup_f32 v74, v78, v74, v23
	v_div_fmas_f32 v23, v79, v89, v93
	s_mov_b64 vcc, s[8:9]
	v_fma_f32 v83, -v86, v95, v87
	v_pk_fma_f32 v[4:5], v[24:25], v[74:75], v[4:5] op_sel_hi:[1,0,1]
	v_pk_fma_f32 v[6:7], v[26:27], v[74:75], v[6:7] op_sel_hi:[1,0,1]
	v_pk_fma_f32 v[8:9], v[28:29], v[74:75], v[8:9] op_sel_hi:[1,0,1]
	v_pk_fma_f32 v[10:11], v[30:31], v[74:75], v[10:11] op_sel_hi:[1,0,1]
	v_pk_fma_f32 v[0:1], v[32:33], v[74:75], v[0:1] op_sel_hi:[1,0,1]
	v_pk_fma_f32 v[2:3], v[34:35], v[74:75], v[2:3] op_sel_hi:[1,0,1]
	v_div_fixup_f32 v24, v23, v75, v65
	v_div_fmas_f32 v23, v82, v90, v94
	s_mov_b64 vcc, s[10:11]
	s_waitcnt vmcnt(8)
	v_pk_fma_f32 v[6:7], v[38:39], v[24:25], v[6:7] op_sel_hi:[1,0,1]
	v_pk_fma_f32 v[4:5], v[36:37], v[24:25], v[4:5] op_sel_hi:[1,0,1]
	s_waitcnt vmcnt(7)
	v_pk_fma_f32 v[10:11], v[42:43], v[24:25], v[10:11] op_sel_hi:[1,0,1]
	v_pk_fma_f32 v[8:9], v[40:41], v[24:25], v[8:9] op_sel_hi:[1,0,1]
	s_waitcnt vmcnt(6)
	v_pk_fma_f32 v[2:3], v[46:47], v[24:25], v[2:3] op_sel_hi:[1,0,1]
	v_pk_fma_f32 v[0:1], v[44:45], v[24:25], v[0:1] op_sel_hi:[1,0,1]
	v_div_fixup_f32 v24, v23, v76, v80
	v_div_fmas_f32 v23, v83, v91, v95
	s_waitcnt vmcnt(5)
	v_pk_fma_f32 v[4:5], v[48:49], v[24:25], v[4:5] op_sel_hi:[1,0,1]
	v_pk_fma_f32 v[6:7], v[50:51], v[24:25], v[6:7] op_sel_hi:[1,0,1]
	s_waitcnt vmcnt(4)
	v_pk_fma_f32 v[8:9], v[52:53], v[24:25], v[8:9] op_sel_hi:[1,0,1]
	v_pk_fma_f32 v[10:11], v[54:55], v[24:25], v[10:11] op_sel_hi:[1,0,1]
	s_waitcnt vmcnt(3)
	v_pk_fma_f32 v[0:1], v[56:57], v[24:25], v[0:1] op_sel_hi:[1,0,1]
	v_pk_fma_f32 v[2:3], v[58:59], v[24:25], v[2:3] op_sel_hi:[1,0,1]
	v_div_fixup_f32 v24, v23, v77, v81
	s_waitcnt vmcnt(2)
	v_pk_fma_f32 v[6:7], v[62:63], v[24:25], v[6:7] op_sel_hi:[1,0,1]
	v_pk_fma_f32 v[4:5], v[60:61], v[24:25], v[4:5] op_sel_hi:[1,0,1]
	s_waitcnt vmcnt(1)
	v_pk_fma_f32 v[10:11], v[68:69], v[24:25], v[10:11] op_sel_hi:[1,0,1]
	v_pk_fma_f32 v[8:9], v[66:67], v[24:25], v[8:9] op_sel_hi:[1,0,1]
	s_waitcnt vmcnt(0)
	v_pk_fma_f32 v[2:3], v[72:73], v[24:25], v[2:3] op_sel_hi:[1,0,1]
	v_pk_fma_f32 v[0:1], v[70:71], v[24:25], v[0:1] op_sel_hi:[1,0,1]
	s_cbranch_scc0 .LBB0_19
	ds_write_b128 v22, v[4:7]
	ds_write_b128 v22, v[8:11] offset:1024
	ds_write_b128 v22, v[0:3] offset:2048
	s_waitcnt lgkmcnt(0)
	s_barrier
	s_and_saveexec_b64 s[6:7], s[2:3]
	s_cbranch_execz .LBB0_17
	ds_read_b128 v[0:3], v13
	ds_read_b128 v[4:7], v13 offset:3072
	ds_read_b128 v[8:11], v13 offset:6144
	ds_read_b128 v[24:27], v13 offset:9216
	s_mul_hi_i32 s8, s22, 0xc000
	s_mul_i32 s22, s22, 0xc000
	s_waitcnt lgkmcnt(2)
	v_pk_add_f32 v[2:3], v[2:3], v[6:7]
	v_pk_add_f32 v[4:5], v[0:1], v[4:5]
	s_waitcnt lgkmcnt(1)
	v_pk_add_f32 v[6:7], v[2:3], v[10:11]
	ds_read_b128 v[0:3], v13 offset:12288
	v_pk_add_f32 v[4:5], v[4:5], v[8:9]
	s_waitcnt lgkmcnt(1)
	v_pk_add_f32 v[8:9], v[6:7], v[26:27]
	v_pk_add_f32 v[18:19], v[4:5], v[24:25]
	ds_read_b128 v[4:7], v13 offset:15360
	s_waitcnt lgkmcnt(1)
	v_pk_add_f32 v[24:25], v[8:9], v[2:3]
	ds_read_b128 v[8:11], v13 offset:18432
	v_pk_add_f32 v[18:19], v[18:19], v[0:1]
	ds_read_b128 v[0:3], v13 offset:21504
	s_add_u32 s9, s5, s22
	s_addc_u32 s10, s17, s8
	s_lshl_b32 s8, s21, 2
	s_waitcnt lgkmcnt(2)
	v_pk_add_f32 v[6:7], v[24:25], v[6:7]
	v_pk_add_f32 v[4:5], v[18:19], v[4:5]
	s_add_u32 s8, s9, s8
	s_waitcnt lgkmcnt(1)
	v_pk_add_f32 v[6:7], v[6:7], v[10:11]
	v_pk_add_f32 v[4:5], v[4:5], v[8:9]
	s_addc_u32 s9, s10, 0
	s_waitcnt lgkmcnt(0)
	v_pk_add_f32 v[2:3], v[6:7], v[2:3]
	v_pk_add_f32 v[0:1], v[4:5], v[0:1]
	v_lshl_add_u64 v[4:5], v[16:17], 2, s[8:9]
	global_store_dwordx4 v[4:5], v[0:3], off
	s_branch .LBB0_17

; #define GAS __attribute__((address_space(1)))
; __device__ __forceinline__ float dot4(f32x4 a, f32x4 b) { return (a.x * b.x + a.y * b.y) + (a.z * b.z + a.w * b.w); }
; __device__ __forceinline__ void phase1(KP kp, LAS unsigned char* lds, int wave, int bid, int G) {
;     ...
;     for (int m = bid * NWAVES + wave; m < T; m += G * NWAVES) {
;         const GAS f32x4* xr = (const GAS f32x4*)(x + (size_t)m * DM) + lane;
;         f32x4 v[8]; float s = 0.f;
; #pragma unroll
;         for (int j = 0; j < 8; ++j) { v[j] = xr[64 * j]; s += dot4(v[j], v[j]); }
.LBB0_135:
	global_load_dwordx4 v[160:163], v[82:83], off offset:-3072 nt
	global_load_dwordx4 v[164:167], v[82:83], off offset:-2048 nt
	global_load_dwordx4 v[168:171], v[82:83], off nt
	global_load_dwordx4 v[172:175], v[82:83], off offset:-1024 nt
	v_add_co_u32_e32 v84, vcc, 0xfffff000, v82
	s_nop 1
	v_addc_co_u32_e32 v85, vcc, -1, v83, vcc
	global_load_dwordx4 v[176:179], v[84:85], off offset:-3072 nt
	global_load_dwordx4 v[180:183], v[84:85], off offset:-2048 nt
	global_load_dwordx4 v[184:187], v[84:85], off offset:-1024 nt
	global_load_dwordx4 v[188:191], v[82:83], off offset:-4096 nt
	v_lshl_add_u64 v[82:83], v[82:83], 0, s[12:13]
	s_waitcnt vmcnt(0)
.Lp1row_loop:
	v_mov_b32_e32 v64, v160
	v_mov_b32_e32 v65, v161
	v_mov_b32_e32 v66, v162
	v_mov_b32_e32 v67, v163
	v_mov_b32_e32 v68, v164
	v_mov_b32_e32 v69, v165
	v_mov_b32_e32 v70, v166
	v_mov_b32_e32 v71, v167
	v_mov_b32_e32 v72, v168
	v_mov_b32_e32 v73, v169
	v_mov_b32_e32 v74, v170
	v_mov_b32_e32 v75, v171
	v_mov_b32_e32 v76, v172
	v_mov_b32_e32 v77, v173
	v_mov_b32_e32 v78, v174
	v_mov_b32_e32 v79, v175
	v_mov_b32_e32 v94, v176
	v_mov_b32_e32 v95, v177
	v_mov_b32_e32 v96, v178
	v_mov_b32_e32 v97, v179
	v_mov_b32_e32 v98, v180
	v_mov_b32_e32 v99, v181
	v_mov_b32_e32 v100, v182
	v_mov_b32_e32 v101, v183
	v_mov_b32_e32 v102, v184
	v_mov_b32_e32 v103, v185
	v_mov_b32_e32 v104, v186
	v_mov_b32_e32 v105, v187
	v_mov_b32_e32 v106, v188
	v_mov_b32_e32 v107, v189
	v_mov_b32_e32 v108, v190
	v_mov_b32_e32 v109, v191
	s_add_i32 s8, s8, s10
	s_cmpk_lt_i32 s8, 0x2000
	s_cbranch_scc0 .Lp1row_nopf
	global_load_dwordx4 v[160:163], v[82:83], off offset:-3072 nt
	global_load_dwordx4 v[164:167], v[82:83], off offset:-2048 nt
	global_load_dwordx4 v[168:171], v[82:83], off nt
	global_load_dwordx4 v[172:175], v[82:83], off offset:-1024 nt
	v_add_co_u32_e32 v84, vcc, 0xfffff000, v82
	s_nop 1
	v_addc_co_u32_e32 v85, vcc, -1, v83, vcc
	global_load_dwordx4 v[176:179], v[84:85], off offset:-3072 nt
	global_load_dwordx4 v[180:183], v[84:85], off offset:-2048 nt
	global_load_dwordx4 v[184:187], v[84:85], off offset:-1024 nt
	global_load_dwordx4 v[188:191], v[82:83], off offset:-4096 nt
	v_lshl_add_u64 v[82:83], v[82:83], 0, s[12:13]
